# touched branch targets of the block switch aligned to 64-byte lines (padding behind unconditional branches)
# baseline (speedup 1.0000x reference)
.Lffc_nocache:
	s_cmp_lt_i32 s26, 4
	global_load_dword v133, v[6:7], off
	global_load_dword v132, v[8:9], off
	global_load_dword v131, v[10:11], off
	global_load_dword v130, v[12:13], off
	global_load_dword v129, v[14:15], off
	global_load_dword v128, v[4:5], off
	v_max_f32_e32 v6, v32, v32
	v_cndmask_b32_e64 v4, v31, v30, s[0:1]
	v_max_f32_e32 v6, 0xc6ea6000, v6
	v_cndmask_b32_e64 v6, v6, 1.0, s[0:1]
	v_and_b32_e32 v7, 0xffff0000, v4
	v_sub_f32_e32 v8, v4, v7
	v_or_b32_sdwa v22, v4, v7 dst_sel:DWORD dst_unused:UNUSED_PAD src0_sel:WORD_1 src1_sel:DWORD
	v_and_b32_e32 v4, 0xffff0000, v6
	v_sub_f32_e32 v7, v6, v4
	v_or_b32_sdwa v24, v6, v4 dst_sel:DWORD dst_unused:UNUSED_PAD src0_sel:WORD_1 src1_sel:DWORD
	v_or_b32_sdwa v23, v8, v4 dst_sel:DWORD dst_unused:UNUSED_PAD src0_sel:WORD_1 src1_sel:DWORD
	v_max_f32_e32 v4, v28, v28
	v_cndmask_b32_e64 v5, v27, v26, s[0:1]
	v_and_b32_e32 v9, 0xffff0000, v7
	v_max_f32_e32 v4, 0xc6ea6000, v4
	v_sub_f32_e32 v9, v7, v9
	v_lshrrev_b32_e32 v7, 16, v7
	v_cndmask_b32_e64 v4, v4, 1.0, s[0:1]
	v_and_b32_e32 v6, 0xffff0000, v5
	v_and_or_b32 v25, v9, s2, v7
	v_sub_f32_e32 v7, v5, v6
	v_or_b32_sdwa v18, v5, v6 dst_sel:DWORD dst_unused:UNUSED_PAD src0_sel:WORD_1 src1_sel:DWORD
	v_and_b32_e32 v5, 0xffff0000, v4
	v_sub_f32_e32 v6, v4, v5
	v_and_b32_e32 v8, 0xffff0000, v6
	v_sub_f32_e32 v8, v6, v8
	v_lshrrev_b32_e32 v6, 16, v6
	v_or_b32_sdwa v20, v4, v5 dst_sel:DWORD dst_unused:UNUSED_PAD src0_sel:WORD_1 src1_sel:DWORD
	v_or_b32_sdwa v19, v7, v5 dst_sel:DWORD dst_unused:UNUSED_PAD src0_sel:WORD_1 src1_sel:DWORD
	v_and_or_b32 v21, v8, s2, v6
	s_mov_b64 s[2:3], 0
	s_cbranch_scc1 .LBB3_11
	s_cmp_gt_i32 s26, 4
	s_cbranch_scc0 .LBB3_14
	s_cmp_gt_i32 s26, 5
	s_cbranch_scc0 .LBB3_15
	s_cmp_eq_u32 s26, 6
	s_mov_b64 s[4:5], 0
	s_cbranch_scc0 .LBB3_48
	v_and_b32_e32 v4, 0xffff0000, v2
	v_max_f32_e32 v3, v3, v3
	v_sub_f32_e32 v4, v2, v4
	v_max_f32_e32 v3, 0xc6ea6000, v3
	v_and_b32_e32 v5, 0xffff0000, v3
	v_and_b32_e32 v4, 0xffff0000, v4
	v_or_b32_sdwa v75, v5, v2 dst_sel:DWORD dst_unused:UNUSED_PAD src0_sel:DWORD src1_sel:WORD_1
	v_or_b32_sdwa v74, v4, v2 dst_sel:DWORD dst_unused:UNUSED_PAD src0_sel:DWORD src1_sel:WORD_1
	v_sub_f32_e32 v2, v3, v5
	v_and_b32_e32 v4, 0xffff0000, v2
	s_mov_b32 s6, 0xffff0000
	v_sub_f32_e32 v4, v2, v4
	v_lshrrev_b32_e32 v2, 16, v2
	v_and_or_b32 v76, v4, s6, v2
	v_or_b32_sdwa v77, v3, v5 dst_sel:DWORD dst_unused:UNUSED_PAD src0_sel:WORD_1 src1_sel:DWORD
	s_movk_i32 s6, 0xfc00
	s_mov_b64 s[8:9], -1
	v_mfma_f32_32x32x16_bf16 v[2:17], v[22:25], v[74:77], 0
	s_nop 11
	v_cvt_pk_f16_f32 v2, v2, v3
	v_cvt_pk_f16_f32 v3, v4, v5
	v_pk_max_i16 v2, v2, s6 op_sel_hi:[1,0]
	v_pk_max_i16 v3, v3, s6 op_sel_hi:[1,0]
	s_nop 0
	v_exp_f16_e32 v43, v2
	v_exp_f16_e32 v45, v3
	v_exp_f16_sdwa v43, v2 dst_sel:WORD_1 dst_unused:UNUSED_PRESERVE src0_sel:WORD_1
	v_exp_f16_sdwa v45, v3 dst_sel:WORD_1 dst_unused:UNUSED_PRESERVE src0_sel:WORD_1
	v_cvt_pk_f16_f32 v2, v6, v7
	v_cvt_pk_f16_f32 v3, v8, v9
	v_pk_max_i16 v2, v2, s6 op_sel_hi:[1,0]
	v_pk_max_i16 v3, v3, s6 op_sel_hi:[1,0]
	s_nop 0
	v_exp_f16_e32 v50, v2
	v_exp_f16_e32 v54, v3
	v_exp_f16_sdwa v50, v2 dst_sel:WORD_1 dst_unused:UNUSED_PRESERVE src0_sel:WORD_1
	v_exp_f16_sdwa v54, v3 dst_sel:WORD_1 dst_unused:UNUSED_PRESERVE src0_sel:WORD_1
	v_cvt_pk_f16_f32 v2, v10, v11
	v_cvt_pk_f16_f32 v3, v12, v13
	v_pk_max_i16 v2, v2, s6 op_sel_hi:[1,0]
	v_pk_max_i16 v3, v3, s6 op_sel_hi:[1,0]
	s_nop 0
	v_exp_f16_e32 v58, v2
	v_exp_f16_e32 v61, v3
	v_exp_f16_sdwa v58, v2 dst_sel:WORD_1 dst_unused:UNUSED_PRESERVE src0_sel:WORD_1
	v_exp_f16_sdwa v61, v3 dst_sel:WORD_1 dst_unused:UNUSED_PRESERVE src0_sel:WORD_1
	v_cvt_pk_f16_f32 v2, v14, v15
	v_cvt_pk_f16_f32 v3, v16, v17
	v_pk_max_i16 v2, v2, s6 op_sel_hi:[1,0]
	v_pk_max_i16 v3, v3, s6 op_sel_hi:[1,0]
	s_nop 0
	v_exp_f16_e32 v64, v2
	v_exp_f16_e32 v66, v3
	v_exp_f16_sdwa v64, v2 dst_sel:WORD_1 dst_unused:UNUSED_PRESERVE src0_sel:WORD_1
	v_exp_f16_sdwa v66, v3 dst_sel:WORD_1 dst_unused:UNUSED_PRESERVE src0_sel:WORD_1
	v_mfma_f32_32x32x16_bf16 v[2:17], v[18:21], v[74:77], 0
	s_nop 11
	v_cvt_pk_f16_f32 v2, v2, v3
	v_cvt_pk_f16_f32 v3, v4, v5
	v_pk_max_i16 v2, v2, s6 op_sel_hi:[1,0]
	v_pk_max_i16 v3, v3, s6 op_sel_hi:[1,0]
	s_nop 0
	v_exp_f16_e32 v72, v2
	v_exp_f16_e32 v76, v3
	v_exp_f16_sdwa v72, v2 dst_sel:WORD_1 dst_unused:UNUSED_PRESERVE src0_sel:WORD_1
	v_exp_f16_sdwa v76, v3 dst_sel:WORD_1 dst_unused:UNUSED_PRESERVE src0_sel:WORD_1
	v_cvt_pk_f16_f32 v2, v6, v7
	v_cvt_pk_f16_f32 v3, v8, v9
	v_pk_max_i16 v2, v2, s6 op_sel_hi:[1,0]
	v_pk_max_i16 v3, v3, s6 op_sel_hi:[1,0]
	s_nop 0
	v_exp_f16_e32 v83, v2
	v_exp_f16_e32 v85, v3
	v_exp_f16_sdwa v83, v2 dst_sel:WORD_1 dst_unused:UNUSED_PRESERVE src0_sel:WORD_1
	v_exp_f16_sdwa v85, v3 dst_sel:WORD_1 dst_unused:UNUSED_PRESERVE src0_sel:WORD_1
	v_cvt_pk_f16_f32 v2, v10, v11
	v_cvt_pk_f16_f32 v3, v12, v13
	v_pk_max_i16 v2, v2, s6 op_sel_hi:[1,0]
	v_pk_max_i16 v3, v3, s6 op_sel_hi:[1,0]
	s_nop 0
	v_exp_f16_e32 v89, v2
	v_exp_f16_e32 v92, v3
	v_exp_f16_sdwa v89, v2 dst_sel:WORD_1 dst_unused:UNUSED_PRESERVE src0_sel:WORD_1
	v_exp_f16_sdwa v92, v3 dst_sel:WORD_1 dst_unused:UNUSED_PRESERVE src0_sel:WORD_1
	v_cvt_pk_f16_f32 v2, v14, v15
	v_cvt_pk_f16_f32 v3, v16, v17
	v_pk_max_i16 v2, v2, s6 op_sel_hi:[1,0]
	v_pk_max_i16 v3, v3, s6 op_sel_hi:[1,0]
	s_nop 0
	v_exp_f16_e32 v95, v2
	v_exp_f16_e32 v96, v3
	v_exp_f16_sdwa v95, v2 dst_sel:WORD_1 dst_unused:UNUSED_PRESERVE src0_sel:WORD_1
	v_exp_f16_sdwa v96, v3 dst_sel:WORD_1 dst_unused:UNUSED_PRESERVE src0_sel:WORD_1
	s_and_b64 vcc, exec, s[4:5]
	s_cbranch_vccnz .LBB3_16
	s_branch .LBB3_17
	.p2align	6

.LBB3_13:
	v_max_f32_e32 v2, v70, v70
	v_max_f32_e32 v2, 0xc6ea6000, v2
	v_and_b32_e32 v4, 0xffff0000, v2
	v_and_b32_e32 v3, 0xffff0000, v68
	v_sub_f32_e32 v5, v2, v4
	v_sub_f32_e32 v3, v68, v3
	v_and_b32_e32 v6, 0xffff0000, v5
	s_mov_b32 s4, 0xffff0000
	v_and_b32_e32 v3, 0xffff0000, v3
	v_sub_f32_e32 v6, v5, v6
	v_lshrrev_b32_e32 v5, 16, v5
	v_or_b32_sdwa v101, v4, v68 dst_sel:DWORD dst_unused:UNUSED_PAD src0_sel:DWORD src1_sel:WORD_1
	v_or_b32_sdwa v100, v3, v68 dst_sel:DWORD dst_unused:UNUSED_PAD src0_sel:DWORD src1_sel:WORD_1
	v_and_or_b32 v102, v6, s4, v5
	v_or_b32_sdwa v103, v2, v4 dst_sel:DWORD dst_unused:UNUSED_PAD src0_sel:WORD_1 src1_sel:DWORD
	s_movk_i32 s4, 0xfc00
	s_nop 0
	v_mfma_f32_32x32x16_bf16 v[2:17], v[22:25], v[100:103], 0
	s_nop 11
	v_cvt_pk_f16_f32 v2, v2, v3
	v_cvt_pk_f16_f32 v3, v4, v5
	v_pk_max_i16 v2, v2, s4 op_sel_hi:[1,0]
	v_pk_max_i16 v3, v3, s4 op_sel_hi:[1,0]
	s_nop 0
	v_exp_f16_e32 v68, v2
	v_exp_f16_e32 v70, v3
	v_exp_f16_sdwa v68, v2 dst_sel:WORD_1 dst_unused:UNUSED_PRESERVE src0_sel:WORD_1
	v_exp_f16_sdwa v70, v3 dst_sel:WORD_1 dst_unused:UNUSED_PRESERVE src0_sel:WORD_1
	v_cvt_pk_f16_f32 v2, v6, v7
	v_cvt_pk_f16_f32 v3, v8, v9
	v_pk_max_i16 v2, v2, s4 op_sel_hi:[1,0]
	v_pk_max_i16 v3, v3, s4 op_sel_hi:[1,0]
	s_nop 0
	v_exp_f16_e32 v71, v2
	v_exp_f16_e32 v73, v3
	v_exp_f16_sdwa v71, v2 dst_sel:WORD_1 dst_unused:UNUSED_PRESERVE src0_sel:WORD_1
	v_exp_f16_sdwa v73, v3 dst_sel:WORD_1 dst_unused:UNUSED_PRESERVE src0_sel:WORD_1
	v_cvt_pk_f16_f32 v2, v10, v11
	v_cvt_pk_f16_f32 v3, v12, v13
	v_pk_max_i16 v2, v2, s4 op_sel_hi:[1,0]
	v_pk_max_i16 v3, v3, s4 op_sel_hi:[1,0]
	s_nop 0
	v_exp_f16_e32 v77, v2
	v_exp_f16_e32 v78, v3
	v_exp_f16_sdwa v77, v2 dst_sel:WORD_1 dst_unused:UNUSED_PRESERVE src0_sel:WORD_1
	v_exp_f16_sdwa v78, v3 dst_sel:WORD_1 dst_unused:UNUSED_PRESERVE src0_sel:WORD_1
	v_cvt_pk_f16_f32 v2, v14, v15
	v_cvt_pk_f16_f32 v3, v16, v17
	v_pk_max_i16 v2, v2, s4 op_sel_hi:[1,0]
	v_pk_max_i16 v3, v3, s4 op_sel_hi:[1,0]
	s_nop 0
	v_exp_f16_e32 v81, v2
	v_exp_f16_e32 v82, v3
	v_exp_f16_sdwa v81, v2 dst_sel:WORD_1 dst_unused:UNUSED_PRESERVE src0_sel:WORD_1
	v_exp_f16_sdwa v82, v3 dst_sel:WORD_1 dst_unused:UNUSED_PRESERVE src0_sel:WORD_1
	v_mfma_f32_32x32x16_bf16 v[2:17], v[18:21], v[100:103], 0
	s_nop 11
	v_cvt_pk_f16_f32 v2, v2, v3
	v_cvt_pk_f16_f32 v3, v4, v5
	v_pk_max_i16 v2, v2, s4 op_sel_hi:[1,0]
	v_pk_max_i16 v3, v3, s4 op_sel_hi:[1,0]
	s_nop 0
	v_exp_f16_e32 v84, v2
	v_exp_f16_e32 v86, v3
	v_exp_f16_sdwa v84, v2 dst_sel:WORD_1 dst_unused:UNUSED_PRESERVE src0_sel:WORD_1
	v_exp_f16_sdwa v86, v3 dst_sel:WORD_1 dst_unused:UNUSED_PRESERVE src0_sel:WORD_1
	v_cvt_pk_f16_f32 v2, v6, v7
	v_cvt_pk_f16_f32 v3, v8, v9
	v_pk_max_i16 v2, v2, s4 op_sel_hi:[1,0]
	v_pk_max_i16 v3, v3, s4 op_sel_hi:[1,0]
	s_nop 0
	v_exp_f16_e32 v87, v2
	v_exp_f16_e32 v88, v3
	v_exp_f16_sdwa v87, v2 dst_sel:WORD_1 dst_unused:UNUSED_PRESERVE src0_sel:WORD_1
	v_exp_f16_sdwa v88, v3 dst_sel:WORD_1 dst_unused:UNUSED_PRESERVE src0_sel:WORD_1
	v_cvt_pk_f16_f32 v2, v10, v11
	v_cvt_pk_f16_f32 v3, v12, v13
	v_pk_max_i16 v2, v2, s4 op_sel_hi:[1,0]
	v_pk_max_i16 v3, v3, s4 op_sel_hi:[1,0]
	s_nop 0
	v_exp_f16_e32 v90, v2
	v_exp_f16_e32 v91, v3
	v_exp_f16_sdwa v90, v2 dst_sel:WORD_1 dst_unused:UNUSED_PRESERVE src0_sel:WORD_1
	v_exp_f16_sdwa v91, v3 dst_sel:WORD_1 dst_unused:UNUSED_PRESERVE src0_sel:WORD_1
	v_cvt_pk_f16_f32 v2, v14, v15
	v_cvt_pk_f16_f32 v3, v16, v17
	v_pk_max_i16 v2, v2, s4 op_sel_hi:[1,0]
	v_pk_max_i16 v3, v3, s4 op_sel_hi:[1,0]
	s_mov_b64 s[4:5], -1
	v_exp_f16_e32 v93, v2
	v_exp_f16_e32 v94, v3
	v_exp_f16_sdwa v93, v2 dst_sel:WORD_1 dst_unused:UNUSED_PRESERVE src0_sel:WORD_1
	v_exp_f16_sdwa v94, v3 dst_sel:WORD_1 dst_unused:UNUSED_PRESERVE src0_sel:WORD_1
	s_andn2_b64 vcc, exec, s[6:7]
	s_cbranch_vccz .LBB3_30
	s_branch .LBB3_31
	.p2align	6

.LBB3_14:
	s_mov_b64 s[4:5], 0
	s_cbranch_execz .LBB3_21
	s_branch .LBB3_20
	.p2align	6

.LBB3_17:
	s_mov_b64 s[6:7], 0
	s_andn2_b64 vcc, exec, s[8:9]
	s_mov_b64 s[4:5], 0
	s_cbranch_vccnz .LBB3_19
	v_max_f32_e32 v2, v48, v48
	v_max_f32_e32 v2, 0xc6ea6000, v2
	v_and_b32_e32 v4, 0xffff0000, v2
	v_and_b32_e32 v3, 0xffff0000, v46
	v_sub_f32_e32 v5, v2, v4
	v_sub_f32_e32 v3, v46, v3
	v_and_b32_e32 v6, 0xffff0000, v5
	s_mov_b32 s4, 0xffff0000
	v_and_b32_e32 v3, 0xffff0000, v3
	v_sub_f32_e32 v6, v5, v6
	v_lshrrev_b32_e32 v5, 16, v5
	v_or_b32_sdwa v47, v4, v46 dst_sel:DWORD dst_unused:UNUSED_PAD src0_sel:DWORD src1_sel:WORD_1
	v_or_b32_sdwa v46, v3, v46 dst_sel:DWORD dst_unused:UNUSED_PAD src0_sel:DWORD src1_sel:WORD_1
	v_and_or_b32 v48, v6, s4, v5
	v_or_b32_sdwa v49, v2, v4 dst_sel:DWORD dst_unused:UNUSED_PAD src0_sel:WORD_1 src1_sel:DWORD
	s_movk_i32 s4, 0xfc00
	s_nop 0
	v_mfma_f32_32x32x16_bf16 v[2:17], v[22:25], v[46:49], 0
	s_nop 11
	v_cvt_pk_f16_f32 v2, v2, v3
	v_cvt_pk_f16_f32 v3, v4, v5
	v_pk_max_i16 v2, v2, s4 op_sel_hi:[1,0]
	v_pk_max_i16 v3, v3, s4 op_sel_hi:[1,0]
	s_nop 0
	v_exp_f16_e32 v26, v2
	v_exp_f16_e32 v27, v3
	v_exp_f16_sdwa v26, v2 dst_sel:WORD_1 dst_unused:UNUSED_PRESERVE src0_sel:WORD_1
	v_exp_f16_sdwa v27, v3 dst_sel:WORD_1 dst_unused:UNUSED_PRESERVE src0_sel:WORD_1
	v_cvt_pk_f16_f32 v2, v6, v7
	v_cvt_pk_f16_f32 v3, v8, v9
	v_pk_max_i16 v2, v2, s4 op_sel_hi:[1,0]
	v_pk_max_i16 v3, v3, s4 op_sel_hi:[1,0]
	s_nop 0
	v_exp_f16_e32 v28, v2
	v_exp_f16_e32 v30, v3
	v_exp_f16_sdwa v28, v2 dst_sel:WORD_1 dst_unused:UNUSED_PRESERVE src0_sel:WORD_1
	v_exp_f16_sdwa v30, v3 dst_sel:WORD_1 dst_unused:UNUSED_PRESERVE src0_sel:WORD_1
	v_cvt_pk_f16_f32 v2, v10, v11
	v_cvt_pk_f16_f32 v3, v12, v13
	v_pk_max_i16 v2, v2, s4 op_sel_hi:[1,0]
	v_pk_max_i16 v3, v3, s4 op_sel_hi:[1,0]
	s_nop 0
	v_exp_f16_e32 v31, v2
	v_exp_f16_e32 v32, v3
	v_exp_f16_sdwa v31, v2 dst_sel:WORD_1 dst_unused:UNUSED_PRESERVE src0_sel:WORD_1
	v_exp_f16_sdwa v32, v3 dst_sel:WORD_1 dst_unused:UNUSED_PRESERVE src0_sel:WORD_1
	v_cvt_pk_f16_f32 v2, v14, v15
	v_cvt_pk_f16_f32 v3, v16, v17
	v_pk_max_i16 v2, v2, s4 op_sel_hi:[1,0]
	v_pk_max_i16 v3, v3, s4 op_sel_hi:[1,0]
	s_nop 0
	v_exp_f16_e32 v39, v2
	v_exp_f16_e32 v40, v3
	v_exp_f16_sdwa v39, v2 dst_sel:WORD_1 dst_unused:UNUSED_PRESERVE src0_sel:WORD_1
	v_exp_f16_sdwa v40, v3 dst_sel:WORD_1 dst_unused:UNUSED_PRESERVE src0_sel:WORD_1
	v_mfma_f32_32x32x16_bf16 v[2:17], v[18:21], v[46:49], 0
	s_nop 11
	v_cvt_pk_f16_f32 v2, v2, v3
	v_cvt_pk_f16_f32 v3, v4, v5
	v_pk_max_i16 v2, v2, s4 op_sel_hi:[1,0]
	v_pk_max_i16 v3, v3, s4 op_sel_hi:[1,0]
	s_nop 0
	v_exp_f16_e32 v41, v2
	v_exp_f16_e32 v42, v3
	v_exp_f16_sdwa v41, v2 dst_sel:WORD_1 dst_unused:UNUSED_PRESERVE src0_sel:WORD_1
	v_exp_f16_sdwa v42, v3 dst_sel:WORD_1 dst_unused:UNUSED_PRESERVE src0_sel:WORD_1
	v_cvt_pk_f16_f32 v2, v6, v7
	v_cvt_pk_f16_f32 v3, v8, v9
	v_pk_max_i16 v2, v2, s4 op_sel_hi:[1,0]
	v_pk_max_i16 v3, v3, s4 op_sel_hi:[1,0]
	s_nop 0
	v_exp_f16_e32 v44, v2
	v_exp_f16_e32 v47, v3
	v_exp_f16_sdwa v44, v2 dst_sel:WORD_1 dst_unused:UNUSED_PRESERVE src0_sel:WORD_1
	v_exp_f16_sdwa v47, v3 dst_sel:WORD_1 dst_unused:UNUSED_PRESERVE src0_sel:WORD_1
	v_cvt_pk_f16_f32 v2, v10, v11
	v_cvt_pk_f16_f32 v3, v12, v13
	v_pk_max_i16 v2, v2, s4 op_sel_hi:[1,0]
	v_pk_max_i16 v3, v3, s4 op_sel_hi:[1,0]
	s_nop 0
	v_exp_f16_e32 v51, v2
	v_exp_f16_e32 v53, v3
	v_exp_f16_sdwa v51, v2 dst_sel:WORD_1 dst_unused:UNUSED_PRESERVE src0_sel:WORD_1
	v_exp_f16_sdwa v53, v3 dst_sel:WORD_1 dst_unused:UNUSED_PRESERVE src0_sel:WORD_1
	v_cvt_pk_f16_f32 v2, v14, v15
	v_cvt_pk_f16_f32 v3, v16, v17
	v_pk_max_i16 v2, v2, s4 op_sel_hi:[1,0]
	v_pk_max_i16 v3, v3, s4 op_sel_hi:[1,0]
	s_mov_b64 s[4:5], -1
	v_exp_f16_e32 v57, v2
	v_exp_f16_e32 v59, v3
	v_exp_f16_sdwa v57, v2 dst_sel:WORD_1 dst_unused:UNUSED_PRESERVE src0_sel:WORD_1
	v_exp_f16_sdwa v59, v3 dst_sel:WORD_1 dst_unused:UNUSED_PRESERVE src0_sel:WORD_1
	s_and_b64 vcc, exec, s[6:7]
	s_cbranch_vccz .LBB3_21
	s_branch .LBB3_20
	.p2align	6

.LBB3_30:
	s_mov_b64 s[4:5], -1
	s_branch .LBB3_31
	.p2align	6

.LBB3_36:
	s_branch .LBB3_37
	.p2align	6

.Lffc_nb0_compute:
	v_max_f32_e32 v2, v135, v135
	v_max_f32_e32 v2, 0xc6ea6000, v2
	v_and_b32_e32 v4, 0xffff0000, v2
	v_and_b32_e32 v3, 0xffff0000, v134
	v_sub_f32_e32 v5, v2, v4
	v_sub_f32_e32 v3, v134, v3
	v_and_b32_e32 v6, 0xffff0000, v5
	s_mov_b32 s2, 0xffff0000
	v_and_b32_e32 v3, 0xffff0000, v3
	v_sub_f32_e32 v6, v5, v6
	v_lshrrev_b32_e32 v5, 16, v5
	v_or_b32_sdwa v125, v4, v134 dst_sel:DWORD dst_unused:UNUSED_PAD src0_sel:DWORD src1_sel:WORD_1
	v_or_b32_sdwa v124, v3, v134 dst_sel:DWORD dst_unused:UNUSED_PAD src0_sel:DWORD src1_sel:WORD_1
	v_and_or_b32 v126, v6, s2, v5
	v_or_b32_sdwa v127, v2, v4 dst_sel:DWORD dst_unused:UNUSED_PAD src0_sel:WORD_1 src1_sel:DWORD
	s_movk_i32 s2, 0xfc00
	s_nop 0
	v_mfma_f32_32x32x16_bf16 v[2:17], v[22:25], v[124:127], 0
	s_nop 11
	v_cvt_pk_f16_f32 v2, v2, v3
	v_cvt_pk_f16_f32 v3, v4, v5
	v_pk_max_i16 v2, v2, s2 op_sel_hi:[1,0]
	v_pk_max_i16 v3, v3, s2 op_sel_hi:[1,0]
	s_nop 0
	v_exp_f16_e32 v117, v2
	v_exp_f16_e32 v113, v3
	v_exp_f16_sdwa v117, v2 dst_sel:WORD_1 dst_unused:UNUSED_PRESERVE src0_sel:WORD_1
	v_exp_f16_sdwa v113, v3 dst_sel:WORD_1 dst_unused:UNUSED_PRESERVE src0_sel:WORD_1
	v_cvt_pk_f16_f32 v2, v6, v7
	v_cvt_pk_f16_f32 v3, v8, v9
	v_pk_max_i16 v2, v2, s2 op_sel_hi:[1,0]
	v_pk_max_i16 v3, v3, s2 op_sel_hi:[1,0]
	s_nop 0
	v_exp_f16_e32 v118, v2
	v_exp_f16_e32 v114, v3
	v_exp_f16_sdwa v118, v2 dst_sel:WORD_1 dst_unused:UNUSED_PRESERVE src0_sel:WORD_1
	v_exp_f16_sdwa v114, v3 dst_sel:WORD_1 dst_unused:UNUSED_PRESERVE src0_sel:WORD_1
	v_cvt_pk_f16_f32 v2, v10, v11
	v_cvt_pk_f16_f32 v3, v12, v13
	v_pk_max_i16 v2, v2, s2 op_sel_hi:[1,0]
	v_pk_max_i16 v3, v3, s2 op_sel_hi:[1,0]
	s_nop 0
	v_exp_f16_e32 v120, v2
	v_exp_f16_e32 v115, v3
	v_exp_f16_sdwa v120, v2 dst_sel:WORD_1 dst_unused:UNUSED_PRESERVE src0_sel:WORD_1
	v_exp_f16_sdwa v115, v3 dst_sel:WORD_1 dst_unused:UNUSED_PRESERVE src0_sel:WORD_1
	v_cvt_pk_f16_f32 v2, v14, v15
	v_cvt_pk_f16_f32 v3, v16, v17
	v_pk_max_i16 v2, v2, s2 op_sel_hi:[1,0]
	v_pk_max_i16 v3, v3, s2 op_sel_hi:[1,0]
	s_nop 0
	v_exp_f16_e32 v122, v2
	v_exp_f16_e32 v116, v3
	v_exp_f16_sdwa v122, v2 dst_sel:WORD_1 dst_unused:UNUSED_PRESERVE src0_sel:WORD_1
	v_exp_f16_sdwa v116, v3 dst_sel:WORD_1 dst_unused:UNUSED_PRESERVE src0_sel:WORD_1
	v_mfma_f32_32x32x16_bf16 v[2:17], v[18:21], v[124:127], 0
	s_nop 11
	v_cvt_pk_f16_f32 v2, v2, v3
	v_cvt_pk_f16_f32 v3, v4, v5
	v_pk_max_i16 v2, v2, s2 op_sel_hi:[1,0]
	v_pk_max_i16 v3, v3, s2 op_sel_hi:[1,0]
	s_nop 0
	v_exp_f16_e32 v124, v2
	v_exp_f16_e32 v119, v3
	v_exp_f16_sdwa v124, v2 dst_sel:WORD_1 dst_unused:UNUSED_PRESERVE src0_sel:WORD_1
	v_exp_f16_sdwa v119, v3 dst_sel:WORD_1 dst_unused:UNUSED_PRESERVE src0_sel:WORD_1
	v_cvt_pk_f16_f32 v2, v6, v7
	v_cvt_pk_f16_f32 v3, v8, v9
	v_pk_max_i16 v2, v2, s2 op_sel_hi:[1,0]
	v_pk_max_i16 v3, v3, s2 op_sel_hi:[1,0]
	s_nop 0
	v_exp_f16_e32 v125, v2
	v_exp_f16_e32 v121, v3
	v_exp_f16_sdwa v125, v2 dst_sel:WORD_1 dst_unused:UNUSED_PRESERVE src0_sel:WORD_1
	v_exp_f16_sdwa v121, v3 dst_sel:WORD_1 dst_unused:UNUSED_PRESERVE src0_sel:WORD_1
	v_cvt_pk_f16_f32 v2, v10, v11
	v_cvt_pk_f16_f32 v3, v12, v13
	v_pk_max_i16 v2, v2, s2 op_sel_hi:[1,0]
	v_pk_max_i16 v3, v3, s2 op_sel_hi:[1,0]
	s_nop 0
	v_exp_f16_e32 v126, v2
	v_exp_f16_e32 v123, v3
	v_exp_f16_sdwa v126, v2 dst_sel:WORD_1 dst_unused:UNUSED_PRESERVE src0_sel:WORD_1
	v_exp_f16_sdwa v123, v3 dst_sel:WORD_1 dst_unused:UNUSED_PRESERVE src0_sel:WORD_1
	v_cvt_pk_f16_f32 v2, v14, v15
	v_cvt_pk_f16_f32 v3, v16, v17
	v_pk_max_i16 v2, v2, s2 op_sel_hi:[1,0]
	v_pk_max_i16 v3, v3, s2 op_sel_hi:[1,0]
	s_nop 0
	v_exp_f16_e32 v127, v2
	v_exp_f16_e32 v17, v3
	v_exp_f16_sdwa v127, v2 dst_sel:WORD_1 dst_unused:UNUSED_PRESERVE src0_sel:WORD_1
	v_exp_f16_sdwa v17, v3 dst_sel:WORD_1 dst_unused:UNUSED_PRESERVE src0_sel:WORD_1
	s_branch .LBB3_39
	.p2align	6

.Lftc_nocache:
	s_cmp_lt_i32 s28, 4
	global_load_dword v133, v[6:7], off
	global_load_dword v132, v[8:9], off
	global_load_dword v131, v[10:11], off
	global_load_dword v130, v[12:13], off
	global_load_dword v129, v[14:15], off
	global_load_dword v128, v[4:5], off
	v_max_f32_e32 v6, v32, v32
	v_cndmask_b32_e64 v4, v31, v30, s[0:1]
	v_max_f32_e32 v6, 0xc6ea6000, v6
	v_cndmask_b32_e64 v6, v6, 1.0, s[0:1]
	v_and_b32_e32 v7, 0xffff0000, v4
	v_sub_f32_e32 v8, v4, v7
	v_or_b32_sdwa v22, v4, v7 dst_sel:DWORD dst_unused:UNUSED_PAD src0_sel:WORD_1 src1_sel:DWORD
	v_and_b32_e32 v4, 0xffff0000, v6
	v_sub_f32_e32 v7, v6, v4
	v_or_b32_sdwa v24, v6, v4 dst_sel:DWORD dst_unused:UNUSED_PAD src0_sel:WORD_1 src1_sel:DWORD
	v_or_b32_sdwa v23, v8, v4 dst_sel:DWORD dst_unused:UNUSED_PAD src0_sel:WORD_1 src1_sel:DWORD
	v_max_f32_e32 v4, v28, v28
	v_cndmask_b32_e64 v5, v27, v26, s[0:1]
	v_and_b32_e32 v9, 0xffff0000, v7
	v_max_f32_e32 v4, 0xc6ea6000, v4
	v_sub_f32_e32 v9, v7, v9
	v_lshrrev_b32_e32 v7, 16, v7
	v_cndmask_b32_e64 v4, v4, 1.0, s[0:1]
	v_and_b32_e32 v6, 0xffff0000, v5
	v_and_or_b32 v25, v9, s2, v7
	v_sub_f32_e32 v7, v5, v6
	v_or_b32_sdwa v18, v5, v6 dst_sel:DWORD dst_unused:UNUSED_PAD src0_sel:WORD_1 src1_sel:DWORD
	v_and_b32_e32 v5, 0xffff0000, v4
	v_sub_f32_e32 v6, v4, v5
	v_and_b32_e32 v8, 0xffff0000, v6
	v_sub_f32_e32 v8, v6, v8
	v_lshrrev_b32_e32 v6, 16, v6
	v_or_b32_sdwa v20, v4, v5 dst_sel:DWORD dst_unused:UNUSED_PAD src0_sel:WORD_1 src1_sel:DWORD
	v_or_b32_sdwa v19, v7, v5 dst_sel:DWORD dst_unused:UNUSED_PAD src0_sel:WORD_1 src1_sel:DWORD
	v_and_or_b32 v21, v8, s2, v6
	s_mov_b64 s[2:3], 0
	s_cbranch_scc1 .LBB4_11
	s_cmp_gt_i32 s28, 4
	s_cbranch_scc0 .LBB4_14
	s_cmp_gt_i32 s28, 5
	s_cbranch_scc0 .LBB4_15
	s_cmp_eq_u32 s28, 6
	s_mov_b64 s[4:5], 0
	s_cbranch_scc0 .LBB4_48
	v_and_b32_e32 v4, 0xffff0000, v2
	v_max_f32_e32 v3, v3, v3
	v_sub_f32_e32 v4, v2, v4
	v_max_f32_e32 v3, 0xc6ea6000, v3
	v_and_b32_e32 v5, 0xffff0000, v3
	v_and_b32_e32 v4, 0xffff0000, v4
	v_or_b32_sdwa v75, v5, v2 dst_sel:DWORD dst_unused:UNUSED_PAD src0_sel:DWORD src1_sel:WORD_1
	v_or_b32_sdwa v74, v4, v2 dst_sel:DWORD dst_unused:UNUSED_PAD src0_sel:DWORD src1_sel:WORD_1
	v_sub_f32_e32 v2, v3, v5
	v_and_b32_e32 v4, 0xffff0000, v2
	s_mov_b32 s6, 0xffff0000
	v_sub_f32_e32 v4, v2, v4
	v_lshrrev_b32_e32 v2, 16, v2
	v_and_or_b32 v76, v4, s6, v2
	v_or_b32_sdwa v77, v3, v5 dst_sel:DWORD dst_unused:UNUSED_PAD src0_sel:WORD_1 src1_sel:DWORD
	s_movk_i32 s6, 0xfc00
	s_mov_b64 s[8:9], -1
	v_mfma_f32_32x32x16_bf16 v[2:17], v[22:25], v[74:77], 0
	s_nop 11
	v_cvt_pk_f16_f32 v2, v2, v3
	v_cvt_pk_f16_f32 v3, v4, v5
	v_pk_max_i16 v2, v2, s6 op_sel_hi:[1,0]
	v_pk_max_i16 v3, v3, s6 op_sel_hi:[1,0]
	s_nop 0
	v_exp_f16_e32 v43, v2
	v_exp_f16_e32 v45, v3
	v_exp_f16_sdwa v43, v2 dst_sel:WORD_1 dst_unused:UNUSED_PRESERVE src0_sel:WORD_1
	v_exp_f16_sdwa v45, v3 dst_sel:WORD_1 dst_unused:UNUSED_PRESERVE src0_sel:WORD_1
	v_cvt_pk_f16_f32 v2, v6, v7
	v_cvt_pk_f16_f32 v3, v8, v9
	v_pk_max_i16 v2, v2, s6 op_sel_hi:[1,0]
	v_pk_max_i16 v3, v3, s6 op_sel_hi:[1,0]
	s_nop 0
	v_exp_f16_e32 v50, v2
	v_exp_f16_e32 v54, v3
	v_exp_f16_sdwa v50, v2 dst_sel:WORD_1 dst_unused:UNUSED_PRESERVE src0_sel:WORD_1
	v_exp_f16_sdwa v54, v3 dst_sel:WORD_1 dst_unused:UNUSED_PRESERVE src0_sel:WORD_1
	v_cvt_pk_f16_f32 v2, v10, v11
	v_cvt_pk_f16_f32 v3, v12, v13
	v_pk_max_i16 v2, v2, s6 op_sel_hi:[1,0]
	v_pk_max_i16 v3, v3, s6 op_sel_hi:[1,0]
	s_nop 0
	v_exp_f16_e32 v58, v2
	v_exp_f16_e32 v61, v3
	v_exp_f16_sdwa v58, v2 dst_sel:WORD_1 dst_unused:UNUSED_PRESERVE src0_sel:WORD_1
	v_exp_f16_sdwa v61, v3 dst_sel:WORD_1 dst_unused:UNUSED_PRESERVE src0_sel:WORD_1
	v_cvt_pk_f16_f32 v2, v14, v15
	v_cvt_pk_f16_f32 v3, v16, v17
	v_pk_max_i16 v2, v2, s6 op_sel_hi:[1,0]
	v_pk_max_i16 v3, v3, s6 op_sel_hi:[1,0]
	s_nop 0
	v_exp_f16_e32 v64, v2
	v_exp_f16_e32 v66, v3
	v_exp_f16_sdwa v64, v2 dst_sel:WORD_1 dst_unused:UNUSED_PRESERVE src0_sel:WORD_1
	v_exp_f16_sdwa v66, v3 dst_sel:WORD_1 dst_unused:UNUSED_PRESERVE src0_sel:WORD_1
	v_mfma_f32_32x32x16_bf16 v[2:17], v[18:21], v[74:77], 0
	s_nop 11
	v_cvt_pk_f16_f32 v2, v2, v3
	v_cvt_pk_f16_f32 v3, v4, v5
	v_pk_max_i16 v2, v2, s6 op_sel_hi:[1,0]
	v_pk_max_i16 v3, v3, s6 op_sel_hi:[1,0]
	s_nop 0
	v_exp_f16_e32 v72, v2
	v_exp_f16_e32 v76, v3
	v_exp_f16_sdwa v72, v2 dst_sel:WORD_1 dst_unused:UNUSED_PRESERVE src0_sel:WORD_1
	v_exp_f16_sdwa v76, v3 dst_sel:WORD_1 dst_unused:UNUSED_PRESERVE src0_sel:WORD_1
	v_cvt_pk_f16_f32 v2, v6, v7
	v_cvt_pk_f16_f32 v3, v8, v9
	v_pk_max_i16 v2, v2, s6 op_sel_hi:[1,0]
	v_pk_max_i16 v3, v3, s6 op_sel_hi:[1,0]
	s_nop 0
	v_exp_f16_e32 v83, v2
	v_exp_f16_e32 v85, v3
	v_exp_f16_sdwa v83, v2 dst_sel:WORD_1 dst_unused:UNUSED_PRESERVE src0_sel:WORD_1
	v_exp_f16_sdwa v85, v3 dst_sel:WORD_1 dst_unused:UNUSED_PRESERVE src0_sel:WORD_1
	v_cvt_pk_f16_f32 v2, v10, v11
	v_cvt_pk_f16_f32 v3, v12, v13
	v_pk_max_i16 v2, v2, s6 op_sel_hi:[1,0]
	v_pk_max_i16 v3, v3, s6 op_sel_hi:[1,0]
	s_nop 0
	v_exp_f16_e32 v89, v2
	v_exp_f16_e32 v92, v3
	v_exp_f16_sdwa v89, v2 dst_sel:WORD_1 dst_unused:UNUSED_PRESERVE src0_sel:WORD_1
	v_exp_f16_sdwa v92, v3 dst_sel:WORD_1 dst_unused:UNUSED_PRESERVE src0_sel:WORD_1
	v_cvt_pk_f16_f32 v2, v14, v15
	v_cvt_pk_f16_f32 v3, v16, v17
	v_pk_max_i16 v2, v2, s6 op_sel_hi:[1,0]
	v_pk_max_i16 v3, v3, s6 op_sel_hi:[1,0]
	s_nop 0
	v_exp_f16_e32 v95, v2
	v_exp_f16_e32 v96, v3
	v_exp_f16_sdwa v95, v2 dst_sel:WORD_1 dst_unused:UNUSED_PRESERVE src0_sel:WORD_1
	v_exp_f16_sdwa v96, v3 dst_sel:WORD_1 dst_unused:UNUSED_PRESERVE src0_sel:WORD_1
	s_and_b64 vcc, exec, s[4:5]
	s_cbranch_vccnz .LBB4_16
	s_branch .LBB4_17
	.p2align	6

.LBB4_39:
	s_waitcnt vmcnt(5)
	v_rcp_f32_e32 v2, v133
	s_waitcnt vmcnt(4)
	v_rcp_f32_e32 v3, v132
	s_waitcnt vmcnt(3)
	v_rcp_f32_e32 v4, v131
	v_cmp_lt_f32_e32 vcc, 0, v133
	s_waitcnt vmcnt(2)
	v_rcp_f32_e32 v5, v130
	s_waitcnt vmcnt(1)
	v_rcp_f32_e32 v6, v129
	v_cndmask_b32_e32 v2, 0, v2, vcc
	v_cmp_lt_f32_e32 vcc, 0, v132
	s_waitcnt vmcnt(0)
	v_rcp_f32_e32 v7, v128
	s_getpc_b64 s[36:37]
	s_sub_u32 s36, s36, 0x9884
	s_subb_u32 s37, s37, 0
	v_lshlrev_b32_e32 v183, 6, v0
	v_min_u32_e32 v183, 0x1d80, v183
	global_load_dword v183, v183, s[36:37]
	v_lshlrev_b32_e32 v182, 6, v38
	global_load_dword v182, v182, s[38:39]
	s_lshl_b32 s40, s29, 10
	s_add_u32 s40, s42, s40
	s_addc_u32 s41, s43, 0
	v_lshlrev_b32_e32 v181, 6, v0
	v_and_b32_e32 v181, 0x7fc0, v181
	global_load_dword v181, v181, s[40:41]
	s_mov_b32 s4, 0x42c80000
	v_cndmask_b32_e32 v3, 0, v3, vcc
	v_cmp_lt_f32_e32 vcc, 0, v131
	v_cmp_ngt_f32_e64 s[2:3], s4, v3
	s_mov_b64 s[6:7], 0
	v_cndmask_b32_e32 v4, 0, v4, vcc
	v_cmp_lt_f32_e32 vcc, 0, v130
	s_nop 1
	v_cndmask_b32_e32 v5, 0, v5, vcc
	v_cmp_lt_f32_e32 vcc, 0, v129
	s_nop 1
	v_cndmask_b32_e32 v6, 0, v6, vcc
	v_cmp_lt_f32_e32 vcc, 0, v128
	s_nop 1
	v_cndmask_b32_e32 v7, 0, v7, vcc
	v_cmp_ngt_f32_e32 vcc, s4, v2
	s_or_b64 s[2:3], vcc, s[2:3]
	v_cmp_ngt_f32_e32 vcc, s4, v4
	s_or_b64 s[2:3], s[2:3], vcc
	v_cmp_ngt_f32_e32 vcc, s4, v5
	s_or_b64 s[2:3], s[2:3], vcc
	v_cmp_ngt_f32_e32 vcc, s4, v6
	s_or_b64 s[2:3], s[2:3], vcc
	v_cmp_ngt_f32_e32 vcc, s4, v7
	s_or_b64 s[2:3], s[2:3], vcc
	v_cndmask_b32_e64 v8, 0, 1, s[2:3]
	v_cmp_ne_u32_e32 vcc, 0, v8
	s_cmp_eq_u64 vcc, 0
	s_cselect_b64 s[2:3], -1, 0
	v_cndmask_b32_e64 v8, 0, 1, s[2:3]
	s_nop 0
	v_readfirstlane_b32 s2, v8
	s_bitcmp0_b32 s2, 0
	s_cbranch_scc0 .LBB4_45
	s_cmp_lt_i32 s28, 4
	s_cbranch_scc1 .LBB4_46
	s_cmp_gt_i32 s28, 4
	s_cbranch_scc0 .LBB4_47
	s_mov_b64 s[4:5], -1
	v_mov_b32_e32 v8, 0
	s_cmp_gt_i32 s28, 5
	v_mov_b32_e32 v167, 0
	v_mov_b32_e32 v166, 0
	v_mov_b32_e32 v165, 0
	v_mov_b32_e32 v164, 0
	v_mov_b32_e32 v162, 0
	v_mov_b32_e32 v160, 0
	v_mov_b32_e32 v159, 0
	v_mov_b32_e32 v157, 0
	v_mov_b32_e32 v151, 0
	v_mov_b32_e32 v149, 0
	v_mov_b32_e32 v147, 0
	v_mov_b32_e32 v146, 0
	v_mov_b32_e32 v144, 0
	v_mov_b32_e32 v143, 0
	v_mov_b32_e32 v152, 0
	v_mov_b32_e32 v153, 0
	v_mov_b32_e32 v154, 0
	v_mov_b32_e32 v155, 0
	v_mov_b32_e32 v156, 0
	v_mov_b32_e32 v158, 0
	v_mov_b32_e32 v161, 0
	v_mov_b32_e32 v163, 0
	v_mov_b32_e32 v168, 0
	v_mov_b32_e32 v169, 0
	v_mov_b32_e32 v170, 0
	v_mov_b32_e32 v171, 0
	v_mov_b32_e32 v172, 0
	v_mov_b32_e32 v173, 0
	v_mov_b32_e32 v174, 0
	v_mov_b32_e32 v145, 0
	v_mov_b32_e32 v148, 0
	v_mov_b32_e32 v150, 0
	s_cbranch_scc0 .LBB4_50
	s_cmp_eq_u32 s28, 6
	s_cbranch_scc0 .LBB4_49
	v_mov_b32_e32 v145, 0
	v_mov_b32_e32 v148, 0
	v_mov_b32_e32 v150, 0
	v_mov_b32_e32 v143, 0
	v_mov_b32_e32 v144, 0
	v_mov_b32_e32 v146, 0
	v_mov_b32_e32 v147, 0
	v_mov_b32_e32 v149, 0
	v_mov_b32_e32 v151, 0
	v_mov_b32_e32 v152, 0
	v_mov_b32_e32 v153, 0
	v_mov_b32_e32 v154, 0
	v_mov_b32_e32 v155, 0
	v_mov_b32_e32 v156, 0
	v_mov_b32_e32 v158, 0
	v_mov_b32_e32 v161, 0
	v_mov_b32_e32 v163, 0
	v_mov_b32_e32 v157, 0
	v_mov_b32_e32 v159, 0
	v_mov_b32_e32 v160, 0
	v_mov_b32_e32 v162, 0
	v_mov_b32_e32 v164, 0
	v_mov_b32_e32 v165, 0
	v_mov_b32_e32 v166, 0
	v_mov_b32_e32 v167, 0
	v_mov_b32_e32 v168, 0
	v_mov_b32_e32 v169, 0
	v_mov_b32_e32 v170, 0
	v_mov_b32_e32 v171, 0
	v_mov_b32_e32 v172, 0
	v_mov_b32_e32 v173, 0
	v_mov_b32_e32 v174, 0
	v_fma_mix_f32 v148, v43, v7, v148 op_sel_hi:[1,0,0]
	v_fma_mix_f32 v150, v45, v7, v150 op_sel_hi:[1,0,0]
	v_fma_mix_f32 v143, v50, v7, v143 op_sel_hi:[1,0,0]
	v_fma_mix_f32 v144, v54, v7, v144 op_sel_hi:[1,0,0]
	v_fma_mix_f32 v146, v58, v7, v146 op_sel_hi:[1,0,0]
	v_fma_mix_f32 v147, v61, v7, v147 op_sel_hi:[1,0,0]
	v_fma_mix_f32 v149, v64, v7, v149 op_sel_hi:[1,0,0]
	v_fma_mix_f32 v151, v66, v7, v151 op_sel_hi:[1,0,0]
	v_fma_mix_f32 v152, v43, v7, v152 op_sel:[1,0,0] op_sel_hi:[1,0,0]
	v_fma_mix_f32 v153, v45, v7, v153 op_sel:[1,0,0] op_sel_hi:[1,0,0]
	v_fma_mix_f32 v154, v50, v7, v154 op_sel:[1,0,0] op_sel_hi:[1,0,0]
	v_fma_mix_f32 v155, v54, v7, v155 op_sel:[1,0,0] op_sel_hi:[1,0,0]
	v_fma_mix_f32 v156, v58, v7, v156 op_sel:[1,0,0] op_sel_hi:[1,0,0]
	v_fma_mix_f32 v158, v61, v7, v158 op_sel:[1,0,0] op_sel_hi:[1,0,0]
	v_fma_mix_f32 v161, v64, v7, v161 op_sel:[1,0,0] op_sel_hi:[1,0,0]
	v_fma_mix_f32 v163, v66, v7, v163 op_sel:[1,0,0] op_sel_hi:[1,0,0]
	v_fma_mix_f32 v157, v72, v7, v157 op_sel_hi:[1,0,0]
	v_fma_mix_f32 v159, v76, v7, v159 op_sel_hi:[1,0,0]
	v_fma_mix_f32 v160, v83, v7, v160 op_sel_hi:[1,0,0]
	v_fma_mix_f32 v162, v85, v7, v162 op_sel_hi:[1,0,0]
	v_fma_mix_f32 v164, v89, v7, v164 op_sel_hi:[1,0,0]
	v_fma_mix_f32 v165, v92, v7, v165 op_sel_hi:[1,0,0]
	v_fma_mix_f32 v166, v95, v7, v166 op_sel_hi:[1,0,0]
	v_fma_mix_f32 v167, v96, v7, v167 op_sel_hi:[1,0,0]
	v_fma_mix_f32 v168, v72, v7, v168 op_sel:[1,0,0] op_sel_hi:[1,0,0]
	v_fma_mix_f32 v169, v76, v7, v169 op_sel:[1,0,0] op_sel_hi:[1,0,0]
	v_fma_mix_f32 v170, v83, v7, v170 op_sel:[1,0,0] op_sel_hi:[1,0,0]
	v_fma_mix_f32 v171, v85, v7, v171 op_sel:[1,0,0] op_sel_hi:[1,0,0]
	v_fma_mix_f32 v172, v89, v7, v172 op_sel:[1,0,0] op_sel_hi:[1,0,0]
	v_fma_mix_f32 v173, v92, v7, v173 op_sel:[1,0,0] op_sel_hi:[1,0,0]
	v_fma_mix_f32 v174, v95, v7, v174 op_sel:[1,0,0] op_sel_hi:[1,0,0]
	v_fma_mix_f32 v145, v96, v7, v145 op_sel:[1,0,0] op_sel_hi:[1,0,0]
	s_branch .LBB4_50
